# v50 + P0 wave specialisation: waves 0-3 do all rmsnorm1 rows while waves 4-7 do all expert-weight e2m3 conversion (two memory streams side by side)
# baseline (speedup 1.0000x reference)
.LBB0_18:
	v_readlane_b32 s0, v255, 3
	v_readlane_b32 s1, v255, 2
	s_lshr_b32 s6, s6, 1
	s_nop 1
	s_lshl_b32 s1, s1, 2
	s_cmp_gt_u32 s0, 3
	s_cbranch_scc1 .Lp0_cvt
	s_add_i32 s24, s1, s0
	s_branch .Lp0_rows
.Lp0_cvt:
	s_add_i32 s24, s1, s0
	s_add_i32 s24, s24, -4
	s_branch .LBB0_21

.LBB0_20:
	global_load_dwordx4 v[14:17], v[4:5], off offset:-3072
	global_load_dwordx4 v[18:21], v[4:5], off offset:-2048
	global_load_dwordx4 v[22:25], v[4:5], off offset:-1024
	global_load_dwordx4 v[26:29], v[4:5], off
	global_load_dwordx4 v[30:33], v[2:3], off
	s_add_i32 s26, s26, s6
	v_lshl_add_u64 v[4:5], v[4:5], 0, s[12:13]
	s_cmp_gt_i32 s26, 0xffff
	s_waitcnt vmcnt(4)
	v_pk_mul_f32 v[34:35], v[16:17], v[16:17]
	v_pk_mul_f32 v[36:37], v[14:15], v[14:15]
	s_waitcnt vmcnt(3)
	v_pk_mul_f32 v[38:39], v[20:21], v[20:21]
	v_pk_mul_f32 v[40:41], v[18:19], v[18:19]
	v_pk_mov_b32 v[46:47], v[36:37], v[34:35] op_sel:[1,0]
	v_mov_b32_e32 v37, v35
	v_pk_mov_b32 v[34:35], v[40:41], v[38:39] op_sel:[1,0]
	v_mov_b32_e32 v41, v39
	s_waitcnt vmcnt(1)
	v_mul_f32_e32 v45, v26, v26
	v_mul_f32_e32 v42, v23, v23
	v_mul_f32_e32 v44, v25, v25
	v_pk_add_f32 v[36:37], v[46:47], v[36:37]
	v_pk_add_f32 v[34:35], v[34:35], v[40:41]
	v_mul_f32_e32 v48, v27, v27
	v_mul_f32_e32 v49, v28, v28
	v_mul_f32_e32 v50, v29, v29
	v_pk_fma_f32 v[38:39], v[22:23], v[22:23], v[42:43] op_sel_hi:[1,1,0]
	v_pk_fma_f32 v[42:43], v[24:25], v[24:25], v[44:45] op_sel_hi:[1,1,0]
	v_pk_add_f32 v[36:37], v[36:37], v[36:37] op_sel:[0,1] op_sel_hi:[1,0]
	v_pk_add_f32 v[34:35], v[34:35], v[34:35] op_sel:[0,1] op_sel_hi:[1,0]
	v_mov_b32_e32 v39, v49
	v_mov_b32_e32 v43, v50
	v_mov_b32_e32 v37, v45
	v_mov_b32_e32 v35, v48
	v_pk_add_f32 v[38:39], v[38:39], v[42:43]
	v_pk_add_f32 v[34:35], v[36:37], v[34:35]
	s_nop 0
	v_pk_add_f32 v[34:35], v[34:35], v[38:39]
	s_nop 0
	v_add_f32_e32 v34, v34, v35
	ds_bpermute_b32 v35, v6, v34
	s_waitcnt lgkmcnt(0)
	v_add_f32_e32 v34, v34, v35
	ds_bpermute_b32 v35, v7, v34
	s_waitcnt lgkmcnt(0)
	v_add_f32_e32 v34, v34, v35
	ds_bpermute_b32 v35, v8, v34
	s_waitcnt lgkmcnt(0)
	v_add_f32_e32 v34, v34, v35
	ds_bpermute_b32 v35, v9, v34
	s_waitcnt lgkmcnt(0)
	v_add_f32_e32 v34, v34, v35
	ds_bpermute_b32 v35, v10, v34
	s_waitcnt lgkmcnt(0)
	v_add_f32_e32 v34, v34, v35
	ds_bpermute_b32 v35, v11, v34
	s_waitcnt lgkmcnt(0)
	v_add_f32_e32 v34, v34, v35
	v_fmamk_f32 v34, v34, 0x3a800000, v12
	v_mul_f32_e32 v35, 0x4f800000, v34
	v_cmp_gt_f32_e32 vcc, s3, v34
	s_nop 1
	v_cndmask_b32_e32 v34, v34, v35, vcc
	v_sqrt_f32_e32 v35, v34
	s_nop 0
	v_add_u32_e32 v36, -1, v35
	v_add_u32_e32 v37, 1, v35
	v_fma_f32 v38, -v36, v35, v34
	v_fma_f32 v39, -v37, v35, v34
	v_cmp_ge_f32_e64 s[0:1], 0, v38
	s_nop 1
	v_cndmask_b32_e64 v35, v35, v36, s[0:1]
	v_cmp_lt_f32_e64 s[0:1], 0, v39
	s_nop 1
	v_cndmask_b32_e64 v35, v35, v37, s[0:1]
	v_mul_f32_e32 v36, 0x37800000, v35
	v_cndmask_b32_e32 v35, v35, v36, vcc
	v_cmp_class_f32_e32 vcc, v34, v13
	s_nop 1
	v_cndmask_b32_e32 v34, v35, v34, vcc
	v_div_scale_f32 v35, s[0:1], v34, v34, 1.0
	v_rcp_f32_e32 v37, v35
	v_div_scale_f32 v36, vcc, 1.0, v34, 1.0
	v_fma_f32 v38, -v35, v37, 1.0
	v_fmac_f32_e32 v37, v38, v37
	v_mul_f32_e32 v38, v36, v37
	v_fma_f32 v39, -v35, v38, v36
	v_fmac_f32_e32 v38, v39, v37
	v_fma_f32 v35, -v35, v38, v36
	v_div_fmas_f32 v35, v35, v37, v38
	v_div_fixup_f32 v34, v35, v34, 1.0
	v_pk_mul_f32 v[14:15], v[14:15], v[34:35] op_sel_hi:[1,0]
	v_pk_mul_f32 v[16:17], v[16:17], v[34:35] op_sel_hi:[1,0]
	s_waitcnt vmcnt(0)
	v_pk_mul_f32 v[14:15], v[30:31], v[14:15]
	v_pk_mul_f32 v[16:17], v[32:33], v[16:17]
	v_bfe_u32 v30, v14, 16, 1
	v_bfe_u32 v32, v16, 16, 1
	v_bfe_u32 v31, v15, 16, 1
	v_bfe_u32 v33, v17, 16, 1
	v_add3_u32 v14, v14, v30, s7
	v_add3_u32 v16, v16, v32, s7
	v_add3_u32 v15, v15, v31, s7
	v_add3_u32 v17, v17, v33, s7
	v_lshrrev_b32_e32 v14, 16, v14
	v_lshrrev_b32_e32 v16, 16, v16
	v_and_or_b32 v14, v15, s25, v14
	v_and_or_b32 v15, v17, s25, v16
	global_store_dwordx2 v[0:1], v[14:15], off
	global_load_dwordx4 v[14:17], v[2:3], off offset:1024
	v_pk_mul_f32 v[18:19], v[18:19], v[34:35] op_sel_hi:[1,0]
	v_pk_mul_f32 v[20:21], v[20:21], v[34:35] op_sel_hi:[1,0]
	s_waitcnt vmcnt(0)
	v_pk_mul_f32 v[14:15], v[14:15], v[18:19]
	v_pk_mul_f32 v[16:17], v[16:17], v[20:21]
	v_bfe_u32 v18, v14, 16, 1
	v_bfe_u32 v20, v16, 16, 1
	v_bfe_u32 v19, v15, 16, 1
	v_bfe_u32 v21, v17, 16, 1
	v_add3_u32 v14, v14, v18, s7
	v_add3_u32 v16, v16, v20, s7
	v_add3_u32 v15, v15, v19, s7
	v_add3_u32 v17, v17, v21, s7
	v_lshrrev_b32_e32 v14, 16, v14
	v_lshrrev_b32_e32 v16, 16, v16
	v_and_or_b32 v14, v15, s25, v14
	v_and_or_b32 v15, v17, s25, v16
	global_store_dwordx2 v[0:1], v[14:15], off offset:512
	global_load_dwordx4 v[14:17], v[2:3], off offset:2048
	v_pk_mul_f32 v[18:19], v[22:23], v[34:35] op_sel_hi:[1,0]
	v_pk_mul_f32 v[20:21], v[24:25], v[34:35] op_sel_hi:[1,0]
	s_waitcnt vmcnt(0)
	v_pk_mul_f32 v[14:15], v[14:15], v[18:19]
	v_pk_mul_f32 v[16:17], v[16:17], v[20:21]
	v_bfe_u32 v18, v14, 16, 1
	v_bfe_u32 v20, v16, 16, 1
	v_bfe_u32 v19, v15, 16, 1
	v_bfe_u32 v21, v17, 16, 1
	v_add3_u32 v14, v14, v18, s7
	v_add3_u32 v16, v16, v20, s7
	v_add3_u32 v15, v15, v19, s7
	v_add3_u32 v17, v17, v21, s7
	v_lshrrev_b32_e32 v14, 16, v14
	v_lshrrev_b32_e32 v16, 16, v16
	v_and_or_b32 v14, v15, s25, v14
	v_and_or_b32 v15, v17, s25, v16
	global_store_dwordx2 v[0:1], v[14:15], off offset:1024
	global_load_dwordx4 v[14:17], v[2:3], off offset:3072
	v_pk_mul_f32 v[18:19], v[26:27], v[34:35] op_sel_hi:[1,0]
	v_pk_mul_f32 v[20:21], v[28:29], v[34:35] op_sel_hi:[1,0]
	s_waitcnt vmcnt(0)
	v_pk_mul_f32 v[14:15], v[14:15], v[18:19]
	v_pk_mul_f32 v[16:17], v[16:17], v[20:21]
	v_bfe_u32 v18, v14, 16, 1
	v_bfe_u32 v20, v16, 16, 1
	v_bfe_u32 v19, v15, 16, 1
	v_bfe_u32 v21, v17, 16, 1
	v_add3_u32 v14, v14, v18, s7
	v_add3_u32 v16, v16, v20, s7
	v_add3_u32 v15, v15, v19, s7
	v_add3_u32 v17, v17, v21, s7
	v_lshrrev_b32_e32 v14, 16, v14
	v_lshrrev_b32_e32 v16, 16, v16
	v_and_or_b32 v14, v15, s25, v14
	v_and_or_b32 v15, v17, s25, v16
	global_store_dwordx2 v[0:1], v[14:15], off offset:1536
	v_lshl_add_u64 v[0:1], v[0:1], 0, s[10:11]
	s_cbranch_scc0 .LBB0_20
	s_branch .LBB0_45
